# grid barrier: non-leader WGs poll TOPGEN directly, leaders skip XGEN bump (one hop less per barrier)
# speedup vs baseline: 1.0136x; 1.0136x over previous
.LBB0_74:
	s_lshl_b32 s3, s75, 8
	s_add_u32 s6, s30, s3
	s_addc_u32 s7, s31, 0
	v_mov_b32_e32 v3, 0x1000
	v_mov_b32_e32 v5, 1
	global_atomic_add v5, v3, v5, s[6:7] offset:1024 sc0
	v_cvt_f32_u32_e32 v3, v4
	v_sub_u32_e32 v6, 0, v4
	v_rcp_iflag_f32_e32 v3, v3
	s_nop 0
	v_mul_f32_e32 v3, 0x4f7ffffe, v3
	v_cvt_u32_f32_e32 v3, v3
	v_mul_lo_u32 v6, v6, v3
	v_mul_hi_u32 v6, v3, v6
	v_add_u32_e32 v3, v3, v6
	s_waitcnt vmcnt(0)
	v_mul_hi_u32 v3, v5, v3
	v_mul_lo_u32 v6, v3, v4
	v_sub_u32_e32 v6, v5, v6
	v_add_u32_e32 v7, 1, v3
	v_cmp_ge_u32_e32 vcc, v6, v4
	v_add_u32_e32 v5, 1, v5
	s_nop 0
	v_cndmask_b32_e32 v3, v3, v7, vcc
	v_sub_u32_e32 v7, v6, v4
	v_cndmask_b32_e32 v6, v6, v7, vcc
	v_add_u32_e32 v7, 1, v3
	v_cmp_ge_u32_e32 vcc, v6, v4
	s_nop 1
	v_cndmask_b32_e32 v3, v3, v7, vcc
	v_mul_lo_u32 v6, v4, v3
	v_add_u32_e32 v4, v6, v4
	v_cmp_ne_u32_e32 vcc, v5, v4
	s_and_saveexec_b64 s[8:9], vcc
	s_xor_b64 s[8:9], exec, s[8:9]
	s_cbranch_execz .LBB0_88
	s_waitcnt lgkmcnt(0)
	v_mov_b32_e32 v2, 0x3500
	global_load_dword v2, v2, s[30:31] sc1
	s_add_u32 s22, s30, 0x3500
	s_addc_u32 s23, s31, 0
	s_waitcnt vmcnt(0)
	v_cmp_eq_u32_e32 vcc, v2, v3
	s_and_saveexec_b64 s[18:19], vcc
	s_cbranch_execz .LBB0_87
	s_mov_b32 s3, 1
	s_mov_b64 s[38:39], 0
	v_mov_b32_e32 v2, 0
	s_branch .LBB0_78

.LBB0_103:
	s_or_b64 exec, exec, s[8:9]
	s_and_saveexec_b64 s[8:9], s[22:23]
	s_cbranch_execz .LBB0_105
	v_mov_b32_e32 v4, 1
	global_atomic_add v[2:3], v4, off
.LBB0_105:
	s_or_b64 exec, exec, s[8:9]
	s_waitcnt vmcnt(0)
	buffer_inv sc1
	s_waitcnt vmcnt(0)
.LBB0_106:
	s_or_b64 exec, exec, s[0:1]
	s_waitcnt lgkmcnt(0)
	s_barrier

.LBB0_132:
	s_lshl_b32 s3, s75, 8
	s_add_u32 s4, s30, s3
	s_addc_u32 s5, s31, 0
	v_mov_b32_e32 v3, 0x1000
	v_mov_b32_e32 v5, 1
	global_atomic_add v5, v3, v5, s[4:5] offset:1024 sc0
	v_cvt_f32_u32_e32 v3, v4
	v_sub_u32_e32 v6, 0, v4
	v_rcp_iflag_f32_e32 v3, v3
	s_nop 0
	v_mul_f32_e32 v3, 0x4f7ffffe, v3
	v_cvt_u32_f32_e32 v3, v3
	v_mul_lo_u32 v6, v6, v3
	v_mul_hi_u32 v6, v3, v6
	v_add_u32_e32 v3, v3, v6
	s_waitcnt vmcnt(0)
	v_mul_hi_u32 v3, v5, v3
	v_mul_lo_u32 v6, v3, v4
	v_sub_u32_e32 v6, v5, v6
	v_add_u32_e32 v7, 1, v3
	v_cmp_ge_u32_e32 vcc, v6, v4
	v_add_u32_e32 v5, 1, v5
	s_nop 0
	v_cndmask_b32_e32 v3, v3, v7, vcc
	v_sub_u32_e32 v7, v6, v4
	v_cndmask_b32_e32 v6, v6, v7, vcc
	v_add_u32_e32 v7, 1, v3
	v_cmp_ge_u32_e32 vcc, v6, v4
	s_nop 1
	v_cndmask_b32_e32 v3, v3, v7, vcc
	v_mul_lo_u32 v6, v4, v3
	v_add_u32_e32 v4, v6, v4
	v_cmp_ne_u32_e32 vcc, v5, v4
	s_and_saveexec_b64 s[8:9], vcc
	s_xor_b64 s[8:9], exec, s[8:9]
	s_cbranch_execz .LBB0_146
	s_waitcnt lgkmcnt(0)
	v_mov_b32_e32 v2, 0x3500
	global_load_dword v2, v2, s[30:31] sc1
	s_add_u32 s22, s30, 0x3500
	s_addc_u32 s23, s31, 0
	s_waitcnt vmcnt(0)
	v_cmp_eq_u32_e32 vcc, v2, v3
	s_and_saveexec_b64 s[18:19], vcc
	s_cbranch_execz .LBB0_145
	s_mov_b32 s3, 1
	s_mov_b64 s[38:39], 0
	v_mov_b32_e32 v2, 0
	s_branch .LBB0_136

.LBB0_161:
	s_or_b64 exec, exec, s[8:9]
	s_and_saveexec_b64 s[8:9], s[22:23]
	s_cbranch_execz .LBB0_163
	v_mov_b32_e32 v4, 1
	global_atomic_add v[2:3], v4, off
.LBB0_163:
	s_or_b64 exec, exec, s[8:9]
	s_waitcnt vmcnt(0)
	buffer_inv sc1
	s_waitcnt vmcnt(0)
.LBB0_164:
	s_or_b64 exec, exec, s[0:1]
	s_waitcnt lgkmcnt(0)
	s_barrier

.LBB0_233:
	s_lshl_b32 s3, s75, 8
	s_add_u32 s6, s30, s3
	s_addc_u32 s7, s31, 0
	v_mov_b32_e32 v3, 0x1000
	v_mov_b32_e32 v5, 1
	global_atomic_add v5, v3, v5, s[6:7] offset:1024 sc0
	v_cvt_f32_u32_e32 v3, v4
	v_sub_u32_e32 v6, 0, v4
	v_rcp_iflag_f32_e32 v3, v3
	s_nop 0
	v_mul_f32_e32 v3, 0x4f7ffffe, v3
	v_cvt_u32_f32_e32 v3, v3
	v_mul_lo_u32 v6, v6, v3
	v_mul_hi_u32 v6, v3, v6
	v_add_u32_e32 v3, v3, v6
	s_waitcnt vmcnt(0)
	v_mul_hi_u32 v3, v5, v3
	v_mul_lo_u32 v6, v3, v4
	v_sub_u32_e32 v6, v5, v6
	v_add_u32_e32 v7, 1, v3
	v_cmp_ge_u32_e32 vcc, v6, v4
	v_add_u32_e32 v5, 1, v5
	s_nop 0
	v_cndmask_b32_e32 v3, v3, v7, vcc
	v_sub_u32_e32 v7, v6, v4
	v_cndmask_b32_e32 v6, v6, v7, vcc
	v_add_u32_e32 v7, 1, v3
	v_cmp_ge_u32_e32 vcc, v6, v4
	s_nop 1
	v_cndmask_b32_e32 v3, v3, v7, vcc
	v_mul_lo_u32 v6, v4, v3
	v_add_u32_e32 v4, v6, v4
	v_cmp_ne_u32_e32 vcc, v5, v4
	s_and_saveexec_b64 s[8:9], vcc
	s_xor_b64 s[8:9], exec, s[8:9]
	s_cbranch_execz .LBB0_247
	s_waitcnt lgkmcnt(0)
	v_mov_b32_e32 v2, 0x3500
	global_load_dword v2, v2, s[30:31] sc1
	s_add_u32 s14, s30, 0x3500
	s_addc_u32 s15, s31, 0
	s_waitcnt vmcnt(0)
	v_cmp_eq_u32_e32 vcc, v2, v3
	s_and_saveexec_b64 s[12:13], vcc
	s_cbranch_execz .LBB0_246
	s_mov_b32 s3, 1
	s_mov_b64 s[18:19], 0
	v_mov_b32_e32 v2, 0
	s_branch .LBB0_237

.LBB0_262:
	s_or_b64 exec, exec, s[8:9]
	s_and_saveexec_b64 s[8:9], s[14:15]
	s_cbranch_execz .LBB0_264
	v_mov_b32_e32 v4, 1
	global_atomic_add v[2:3], v4, off
.LBB0_264:
	s_or_b64 exec, exec, s[8:9]
	s_waitcnt vmcnt(0)
	buffer_inv sc1
	s_waitcnt vmcnt(0)
.LBB0_265:
	s_or_b64 exec, exec, s[4:5]
	s_waitcnt lgkmcnt(0)
	s_barrier

.LBB0_288:
	s_lshl_b32 s3, s75, 8
	s_add_u32 s8, s30, s3
	s_addc_u32 s9, s31, 0
	v_mov_b32_e32 v3, 0x1000
	v_mov_b32_e32 v5, 1
	global_atomic_add v5, v3, v5, s[8:9] offset:1024 sc0
	v_cvt_f32_u32_e32 v3, v4
	v_sub_u32_e32 v6, 0, v4
	v_rcp_iflag_f32_e32 v3, v3
	s_nop 0
	v_mul_f32_e32 v3, 0x4f7ffffe, v3
	v_cvt_u32_f32_e32 v3, v3
	v_mul_lo_u32 v6, v6, v3
	v_mul_hi_u32 v6, v3, v6
	v_add_u32_e32 v3, v3, v6
	s_waitcnt vmcnt(0)
	v_mul_hi_u32 v3, v5, v3
	v_mul_lo_u32 v6, v3, v4
	v_sub_u32_e32 v6, v5, v6
	v_add_u32_e32 v7, 1, v3
	v_cmp_ge_u32_e32 vcc, v6, v4
	v_add_u32_e32 v5, 1, v5
	s_nop 0
	v_cndmask_b32_e32 v3, v3, v7, vcc
	v_sub_u32_e32 v7, v6, v4
	v_cndmask_b32_e32 v6, v6, v7, vcc
	v_add_u32_e32 v7, 1, v3
	v_cmp_ge_u32_e32 vcc, v6, v4
	s_nop 1
	v_cndmask_b32_e32 v3, v3, v7, vcc
	v_mul_lo_u32 v6, v4, v3
	v_add_u32_e32 v4, v6, v4
	v_cmp_ne_u32_e32 vcc, v5, v4
	s_and_saveexec_b64 s[12:13], vcc
	s_xor_b64 s[12:13], exec, s[12:13]
	s_cbranch_execz .LBB0_302
	s_waitcnt lgkmcnt(0)
	v_mov_b32_e32 v2, 0x3500
	global_load_dword v2, v2, s[30:31] sc1
	s_add_u32 s18, s30, 0x3500
	s_addc_u32 s19, s31, 0
	s_waitcnt vmcnt(0)
	v_cmp_eq_u32_e32 vcc, v2, v3
	s_and_saveexec_b64 s[14:15], vcc
	s_cbranch_execz .LBB0_301
	s_mov_b32 s3, 1
	s_mov_b64 s[22:23], 0
	v_mov_b32_e32 v2, 0
	s_branch .LBB0_292

.LBB0_317:
	s_or_b64 exec, exec, s[12:13]
	s_and_saveexec_b64 s[12:13], s[18:19]
	s_cbranch_execz .LBB0_319
	v_mov_b32_e32 v4, 1
	global_atomic_add v[2:3], v4, off
.LBB0_319:
	s_or_b64 exec, exec, s[12:13]
	s_waitcnt vmcnt(0)
	buffer_inv sc1
	s_waitcnt vmcnt(0)
.LBB0_320:
	s_or_b64 exec, exec, s[4:5]
	s_waitcnt lgkmcnt(0)
	s_barrier

.LBB0_383:
	s_or_b64 exec, exec, s[12:13]
	s_and_saveexec_b64 s[12:13], s[18:19]
	s_cbranch_execz .LBB0_385
	v_mov_b32_e32 v4, 1
	global_atomic_add v[2:3], v4, off
.LBB0_385:
	s_or_b64 exec, exec, s[12:13]
	s_waitcnt vmcnt(0)
	buffer_inv sc1
	s_waitcnt vmcnt(0)
.LBB0_386:
	s_or_b64 exec, exec, s[4:5]
	s_waitcnt lgkmcnt(0)
	s_barrier

.LBB0_418:
	s_lshl_b32 s3, s75, 8
	s_add_u32 s6, s30, s3
	s_addc_u32 s7, s31, 0
	v_mov_b32_e32 v2, 0x1000
	v_mov_b32_e32 v4, 1
	global_atomic_add v4, v2, v4, s[6:7] offset:1024 sc0
	v_cvt_f32_u32_e32 v2, v3
	v_sub_u32_e32 v5, 0, v3
	v_rcp_iflag_f32_e32 v2, v2
	s_nop 0
	v_mul_f32_e32 v2, 0x4f7ffffe, v2
	v_cvt_u32_f32_e32 v2, v2
	v_mul_lo_u32 v5, v5, v2
	v_mul_hi_u32 v5, v2, v5
	v_add_u32_e32 v2, v2, v5
	s_waitcnt vmcnt(0)
	v_mul_hi_u32 v2, v4, v2
	v_mul_lo_u32 v5, v2, v3
	v_sub_u32_e32 v5, v4, v5
	v_add_u32_e32 v6, 1, v2
	v_cmp_ge_u32_e32 vcc, v5, v3
	v_add_u32_e32 v4, 1, v4
	s_nop 0
	v_cndmask_b32_e32 v2, v2, v6, vcc
	v_sub_u32_e32 v6, v5, v3
	v_cndmask_b32_e32 v5, v5, v6, vcc
	v_add_u32_e32 v6, 1, v2
	v_cmp_ge_u32_e32 vcc, v5, v3
	s_nop 1
	v_cndmask_b32_e32 v2, v2, v6, vcc
	v_mul_lo_u32 v5, v3, v2
	v_add_u32_e32 v3, v5, v3
	v_cmp_ne_u32_e32 vcc, v4, v3
	s_and_saveexec_b64 s[8:9], vcc
	s_xor_b64 s[8:9], exec, s[8:9]
	s_cbranch_execz .LBB0_432
	s_waitcnt lgkmcnt(0)
	v_mov_b32_e32 v1, 0x3500
	global_load_dword v1, v1, s[30:31] sc1
	s_add_u32 s14, s30, 0x3500
	s_addc_u32 s15, s31, 0
	s_waitcnt vmcnt(0)
	v_cmp_eq_u32_e32 vcc, v1, v2
	s_and_saveexec_b64 s[12:13], vcc
	s_cbranch_execz .LBB0_431
	s_mov_b32 s3, 1
	s_mov_b64 s[18:19], 0
	v_mov_b32_e32 v1, 0
	s_branch .LBB0_422

.LBB0_447:
	s_or_b64 exec, exec, s[8:9]
	s_and_saveexec_b64 s[8:9], s[14:15]
	s_cbranch_execz .LBB0_449
	v_mov_b32_e32 v1, 1
	global_atomic_add v[2:3], v1, off
.LBB0_449:
	s_or_b64 exec, exec, s[8:9]
	s_waitcnt vmcnt(0)
	buffer_inv sc1
	s_waitcnt vmcnt(0)
.LBB0_450:
	s_or_b64 exec, exec, s[4:5]
	s_waitcnt lgkmcnt(0)
	s_barrier

.LBB0_528:
	s_or_b64 exec, exec, s[8:9]
	s_and_saveexec_b64 s[8:9], s[14:15]
	s_cbranch_execz .LBB0_530
	v_mov_b32_e32 v1, 1
	global_atomic_add v[2:3], v1, off
.LBB0_530:
	s_or_b64 exec, exec, s[8:9]
	s_waitcnt vmcnt(0)
	buffer_inv sc1
	s_waitcnt vmcnt(0)
.LBB0_531:
	s_or_b64 exec, exec, s[4:5]
	s_waitcnt lgkmcnt(0)
	s_barrier

.LBB0_603:
	s_or_b64 exec, exec, s[8:9]
	s_and_saveexec_b64 s[8:9], s[14:15]
	s_cbranch_execz .LBB0_605
	v_mov_b32_e32 v1, 1
	global_atomic_add v[2:3], v1, off
.LBB0_605:
	s_or_b64 exec, exec, s[8:9]
	s_waitcnt vmcnt(0)
	buffer_inv sc1
	s_waitcnt vmcnt(0)
.LBB0_606:
	s_or_b64 exec, exec, s[4:5]
	s_waitcnt lgkmcnt(0)
	s_barrier

.LBB0_640:
	s_lshl_b32 s4, s75, 8
	s_add_u32 s4, s30, s4
	s_addc_u32 s5, s31, 0
	v_mov_b32_e32 v2, 0x1000
	v_mov_b32_e32 v4, 1
	global_atomic_add v4, v2, v4, s[4:5] offset:1024 sc0
	v_cvt_f32_u32_e32 v2, v3
	v_sub_u32_e32 v5, 0, v3
	v_rcp_iflag_f32_e32 v2, v2
	s_nop 0
	v_mul_f32_e32 v2, 0x4f7ffffe, v2
	v_cvt_u32_f32_e32 v2, v2
	v_mul_lo_u32 v5, v5, v2
	v_mul_hi_u32 v5, v2, v5
	v_add_u32_e32 v2, v2, v5
	s_waitcnt vmcnt(0)
	v_mul_hi_u32 v2, v4, v2
	v_mul_lo_u32 v5, v2, v3
	v_sub_u32_e32 v5, v4, v5
	v_add_u32_e32 v6, 1, v2
	v_cmp_ge_u32_e32 vcc, v5, v3
	v_add_u32_e32 v4, 1, v4
	s_nop 0
	v_cndmask_b32_e32 v2, v2, v6, vcc
	v_sub_u32_e32 v6, v5, v3
	v_cndmask_b32_e32 v5, v5, v6, vcc
	v_add_u32_e32 v6, 1, v2
	v_cmp_ge_u32_e32 vcc, v5, v3
	s_nop 1
	v_cndmask_b32_e32 v2, v2, v6, vcc
	v_mul_lo_u32 v5, v3, v2
	v_add_u32_e32 v3, v5, v3
	v_cmp_ne_u32_e32 vcc, v4, v3
	s_and_saveexec_b64 s[6:7], vcc
	s_xor_b64 s[6:7], exec, s[6:7]
	s_cbranch_execz .LBB0_654
	s_waitcnt lgkmcnt(0)
	v_mov_b32_e32 v1, 0x3500
	global_load_dword v1, v1, s[30:31] sc1
	s_add_u32 s12, s30, 0x3500
	s_addc_u32 s13, s31, 0
	s_waitcnt vmcnt(0)
	v_cmp_eq_u32_e32 vcc, v1, v2
	s_and_saveexec_b64 s[8:9], vcc
	s_cbranch_execz .LBB0_653
	s_mov_b32 s24, 1
	s_mov_b64 s[14:15], 0
	v_mov_b32_e32 v1, 0
	s_branch .LBB0_644

.LBB0_671:
	s_or_b64 exec, exec, s[6:7]
	s_waitcnt vmcnt(0)
	buffer_inv sc1
	s_waitcnt vmcnt(0)

.LBB0_892:
	s_lshl_b32 s4, s75, 8
	s_add_u32 s4, s30, s4
	s_addc_u32 s5, s31, 0
	v_mov_b32_e32 v1, 0x1000
	v_mov_b32_e32 v3, 1
	global_atomic_add v3, v1, v3, s[4:5] offset:1024 sc0
	v_cvt_f32_u32_e32 v1, v2
	v_sub_u32_e32 v4, 0, v2
	v_rcp_iflag_f32_e32 v1, v1
	s_nop 0
	v_mul_f32_e32 v1, 0x4f7ffffe, v1
	v_cvt_u32_f32_e32 v1, v1
	v_mul_lo_u32 v4, v4, v1
	v_mul_hi_u32 v4, v1, v4
	v_add_u32_e32 v1, v1, v4
	s_waitcnt vmcnt(0)
	v_mul_hi_u32 v1, v3, v1
	v_mul_lo_u32 v4, v1, v2
	v_sub_u32_e32 v4, v3, v4
	v_add_u32_e32 v5, 1, v1
	v_cmp_ge_u32_e32 vcc, v4, v2
	v_add_u32_e32 v3, 1, v3
	s_nop 0
	v_cndmask_b32_e32 v1, v1, v5, vcc
	v_sub_u32_e32 v5, v4, v2
	v_cndmask_b32_e32 v4, v4, v5, vcc
	v_add_u32_e32 v5, 1, v1
	v_cmp_ge_u32_e32 vcc, v4, v2
	s_nop 1
	v_cndmask_b32_e32 v1, v1, v5, vcc
	v_mul_lo_u32 v4, v2, v1
	v_add_u32_e32 v2, v4, v2
	v_cmp_ne_u32_e32 vcc, v3, v2
	s_and_saveexec_b64 s[6:7], vcc
	s_xor_b64 s[6:7], exec, s[6:7]
	s_cbranch_execz .LBB0_921
	s_waitcnt lgkmcnt(0)
	v_mov_b32_e32 v0, 0x3500
	global_load_dword v0, v0, s[30:31] sc1
	s_add_u32 s12, s30, 0x3500
	s_addc_u32 s13, s31, 0
	s_waitcnt vmcnt(0)
	v_cmp_eq_u32_e32 vcc, v0, v1
	s_and_saveexec_b64 s[8:9], vcc
	s_cbranch_execz .LBB0_920
	s_mov_b32 s24, 1
	s_mov_b64 s[14:15], 0
	v_mov_b32_e32 v0, 0
	s_branch .LBB0_896
